# counted lgkmcnt waits extended to the 16-fragment shared-K batches of the selected and window branches (the author's lgkmcnt(8) + compiler lgkmcnt(0) replaced)
# baseline (speedup 1.0000x reference)
.LBB0_1160:
	s_and_b64 vcc, exec, s[6:7]
	s_cbranch_vccz .LBB0_1167
	s_add_i32 s0, s9, s8
	v_add_u32_e32 v4, s0, v145
	v_add_u32_e32 v5, s0, v144
	v_add_u32_e32 v130, s0, v143
	v_add_u32_e32 v131, s0, v142
	ds_read_b128 v[38:41], v4
	ds_read_b128 v[42:45], v4 offset:4096
	ds_read_b128 v[46:49], v5
	ds_read_b128 v[50:53], v5 offset:4096
	ds_read_b128 v[118:121], v130
	ds_read_b128 v[126:129], v130 offset:4096
	ds_read_b128 v[122:125], v131
	ds_read_b128 v[138:141], v131 offset:4096
	ds_read_b128 v[142:145], v4 offset:8192
	ds_read_b128 v[146:149], v4 offset:12288
	ds_read_b128 v[150:153], v5 offset:8192
	ds_read_b128 v[154:157], v5 offset:12288
	ds_read_b128 v[158:161], v130 offset:8192
	ds_read_b128 v[162:165], v130 offset:12288
	ds_read_b128 v[168:171], v131 offset:8192
	ds_read_b128 v[204:207], v131 offset:12288

	s_setprio 1
	s_waitcnt lgkmcnt(15)
	v_mfma_f32_16x16x32_f16 v[130:133], v[38:41], v[6:9], 0
	v_mfma_f32_16x16x32_f16 v[38:41], v[38:41], v[22:25], 0
	s_waitcnt lgkmcnt(13)
	v_mfma_f32_16x16x32_f16 v[130:133], v[46:49], v[10:13], v[130:133]
	v_mfma_f32_16x16x32_f16 v[38:41], v[46:49], v[26:29], v[38:41]
	s_waitcnt lgkmcnt(11)
	v_mfma_f32_16x16x32_f16 v[46:49], v[118:121], v[14:17], v[130:133]
	v_mfma_f32_16x16x32_f16 v[38:41], v[118:121], v[30:33], v[38:41]
	s_waitcnt lgkmcnt(9)
	v_mfma_f32_16x16x32_f16 v[130:133], v[122:125], v[18:21], v[46:49]
	v_mfma_f32_16x16x32_f16 v[122:125], v[122:125], v[34:37], v[38:41]
	v_mfma_f32_16x16x32_f16 v[38:41], v[42:45], v[6:9], 0
	v_mfma_f32_16x16x32_f16 v[42:45], v[42:45], v[22:25], 0
	v_mfma_f32_16x16x32_f16 v[38:41], v[50:53], v[10:13], v[38:41]
	v_mfma_f32_16x16x32_f16 v[42:45], v[50:53], v[26:29], v[42:45]
	v_mfma_f32_16x16x32_f16 v[38:41], v[126:129], v[14:17], v[38:41]
	v_mfma_f32_16x16x32_f16 v[42:45], v[126:129], v[30:33], v[42:45]
	s_waitcnt lgkmcnt(8)
	v_mfma_f32_16x16x32_f16 v[38:41], v[138:141], v[18:21], v[38:41]
	v_mfma_f32_16x16x32_f16 v[46:49], v[138:141], v[34:37], v[42:45]
	s_waitcnt lgkmcnt(7)
	v_mfma_f32_16x16x32_f16 v[42:45], v[142:145], v[6:9], 0
	v_mfma_f32_16x16x32_f16 v[50:53], v[142:145], v[22:25], 0
	s_waitcnt lgkmcnt(5)
	v_mfma_f32_16x16x32_f16 v[42:45], v[150:153], v[10:13], v[42:45]
	v_mfma_f32_16x16x32_f16 v[50:53], v[150:153], v[26:29], v[50:53]
	s_waitcnt lgkmcnt(3)
	v_mfma_f32_16x16x32_f16 v[42:45], v[158:161], v[14:17], v[42:45]
	v_mfma_f32_16x16x32_f16 v[50:53], v[158:161], v[30:33], v[50:53]
	s_waitcnt lgkmcnt(1)
	v_mfma_f32_16x16x32_f16 v[126:129], v[168:171], v[18:21], v[42:45]
	v_mfma_f32_16x16x32_f16 v[118:121], v[168:171], v[34:37], v[50:53]
	v_mfma_f32_16x16x32_f16 v[42:45], v[146:149], v[6:9], 0
	v_mfma_f32_16x16x32_f16 v[50:53], v[146:149], v[22:25], 0
	v_mfma_f32_16x16x32_f16 v[42:45], v[154:157], v[10:13], v[42:45]
	v_mfma_f32_16x16x32_f16 v[50:53], v[154:157], v[26:29], v[50:53]
	v_mfma_f32_16x16x32_f16 v[42:45], v[162:165], v[14:17], v[42:45]
	v_mfma_f32_16x16x32_f16 v[50:53], v[162:165], v[30:33], v[50:53]
	s_waitcnt lgkmcnt(0)
	v_mfma_f32_16x16x32_f16 v[42:45], v[204:207], v[18:21], v[42:45]
	v_mfma_f32_16x16x32_f16 v[50:53], v[204:207], v[34:37], v[50:53]
	s_setprio 0
	v_max_f32_e32 v4, v131, v131
	v_max_f32_e32 v5, v130, v130
	v_max_f32_e32 v4, v5, v4
	v_max3_f32 v4, v4, v132, v133
	v_max3_f32 v4, v4, v38, v39
	v_max3_f32 v4, v4, v40, v41
	v_max3_f32 v4, v4, v126, v127
	v_max3_f32 v4, v4, v128, v129
	v_and_b32_e32 v2, 1, v2
	v_max3_f32 v4, v4, v42, v43
	v_max3_f32 v4, v4, v44, v45
	v_cmp_eq_u32_e32 vcc, 1, v2
	v_mul_f32_e32 v172, 0x3e0293ee, v4
	v_mov_b32_e32 v143, v136
	v_cndmask_b32_e32 v142, v241, v180, vcc
	v_pk_add_f32 v[138:139], v[142:143], v[172:173]
	v_mov_b32_e32 v4, 1.0
	v_cmp_gt_f32_e32 vcc, v138, v139
	s_cbranch_vccz .LBB0_1163
	ds_bpermute_b32 v2, v245, v138
	v_max_f32_e32 v5, v138, v138
	v_mov_b32_e32 v139, v137
	s_waitcnt lgkmcnt(0)
	v_max_f32_e32 v2, v2, v2
	v_max_f32_e32 v2, v5, v2
	ds_bpermute_b32 v5, v246, v2
	s_waitcnt lgkmcnt(0)
	v_max3_f32 v138, v136, v2, v5
	v_sub_f32_e32 v2, v136, v138
	v_exp_f32_e32 v194, v2
	v_mov_b32_e32 v136, v138
	s_branch .LBB0_1164

.LBB0_1230:
	s_and_b64 vcc, exec, s[6:7]
	s_cbranch_vccz .LBB0_1237
	s_add_i32 s6, s15, s47
	v_add_u32_e32 v4, s6, v143
	v_add_u32_e32 v5, s6, v142
	v_add_u32_e32 v2, s6, v2
	v_add_u32_e32 v1, s6, v1
	ds_read_b128 v[38:41], v4
	ds_read_b128 v[42:45], v4 offset:4096
	ds_read_b128 v[46:49], v5
	ds_read_b128 v[50:53], v5 offset:4096
	ds_read_b128 v[118:121], v2
	ds_read_b128 v[126:129], v2 offset:4096
	ds_read_b128 v[122:125], v1
	ds_read_b128 v[138:141], v1 offset:4096
	ds_read_b128 v[142:145], v4 offset:8192
	ds_read_b128 v[146:149], v4 offset:12288
	ds_read_b128 v[150:153], v5 offset:8192
	ds_read_b128 v[154:157], v5 offset:12288
	ds_read_b128 v[158:161], v2 offset:8192
	ds_read_b128 v[162:165], v2 offset:12288
	ds_read_b128 v[168:171], v1 offset:8192
	ds_read_b128 v[194:197], v1 offset:12288

	s_setprio 1
	s_waitcnt lgkmcnt(15)
	v_mfma_f32_16x16x32_f16 v[130:133], v[38:41], v[6:9], 0
	v_mfma_f32_16x16x32_f16 v[38:41], v[38:41], v[22:25], 0
	s_waitcnt lgkmcnt(13)
	v_mfma_f32_16x16x32_f16 v[130:133], v[46:49], v[10:13], v[130:133]
	v_mfma_f32_16x16x32_f16 v[38:41], v[46:49], v[26:29], v[38:41]
	s_waitcnt lgkmcnt(11)
	v_mfma_f32_16x16x32_f16 v[46:49], v[118:121], v[14:17], v[130:133]
	v_mfma_f32_16x16x32_f16 v[38:41], v[118:121], v[30:33], v[38:41]
	s_waitcnt lgkmcnt(9)
	v_mfma_f32_16x16x32_f16 v[130:133], v[122:125], v[18:21], v[46:49]
	v_mfma_f32_16x16x32_f16 v[122:125], v[122:125], v[34:37], v[38:41]
	v_mfma_f32_16x16x32_f16 v[38:41], v[42:45], v[6:9], 0
	v_mfma_f32_16x16x32_f16 v[42:45], v[42:45], v[22:25], 0
	v_mfma_f32_16x16x32_f16 v[38:41], v[50:53], v[10:13], v[38:41]
	v_mfma_f32_16x16x32_f16 v[42:45], v[50:53], v[26:29], v[42:45]
	v_mfma_f32_16x16x32_f16 v[38:41], v[126:129], v[14:17], v[38:41]
	v_mfma_f32_16x16x32_f16 v[42:45], v[126:129], v[30:33], v[42:45]
	s_waitcnt lgkmcnt(8)
	v_mfma_f32_16x16x32_f16 v[38:41], v[138:141], v[18:21], v[38:41]
	v_mfma_f32_16x16x32_f16 v[46:49], v[138:141], v[34:37], v[42:45]
	s_waitcnt lgkmcnt(7)
	v_mfma_f32_16x16x32_f16 v[42:45], v[142:145], v[6:9], 0
	v_mfma_f32_16x16x32_f16 v[50:53], v[142:145], v[22:25], 0
	s_waitcnt lgkmcnt(5)
	v_mfma_f32_16x16x32_f16 v[42:45], v[150:153], v[10:13], v[42:45]
	v_mfma_f32_16x16x32_f16 v[50:53], v[150:153], v[26:29], v[50:53]
	s_waitcnt lgkmcnt(3)
	v_mfma_f32_16x16x32_f16 v[42:45], v[158:161], v[14:17], v[42:45]
	v_mfma_f32_16x16x32_f16 v[50:53], v[158:161], v[30:33], v[50:53]
	s_waitcnt lgkmcnt(1)
	v_mfma_f32_16x16x32_f16 v[126:129], v[168:171], v[18:21], v[42:45]
	v_mfma_f32_16x16x32_f16 v[118:121], v[168:171], v[34:37], v[50:53]
	v_mfma_f32_16x16x32_f16 v[42:45], v[146:149], v[6:9], 0
	v_mfma_f32_16x16x32_f16 v[50:53], v[146:149], v[22:25], 0
	v_mfma_f32_16x16x32_f16 v[42:45], v[154:157], v[10:13], v[42:45]
	v_mfma_f32_16x16x32_f16 v[50:53], v[154:157], v[26:29], v[50:53]
	v_mfma_f32_16x16x32_f16 v[42:45], v[162:165], v[14:17], v[42:45]
	v_mfma_f32_16x16x32_f16 v[50:53], v[162:165], v[30:33], v[50:53]
	s_waitcnt lgkmcnt(0)
	v_mfma_f32_16x16x32_f16 v[42:45], v[194:197], v[18:21], v[42:45]
	v_mfma_f32_16x16x32_f16 v[50:53], v[194:197], v[34:37], v[50:53]
	s_setprio 0
	v_max_f32_e32 v1, v131, v131
	v_max_f32_e32 v2, v130, v130
	v_max_f32_e32 v1, v2, v1
	v_max3_f32 v1, v1, v132, v133
	v_max3_f32 v1, v1, v38, v39
	v_max3_f32 v1, v1, v40, v41
	v_max3_f32 v1, v1, v126, v127
	v_max3_f32 v1, v1, v128, v129
	v_max3_f32 v1, v1, v42, v43
	v_max3_f32 v1, v1, v44, v45
	v_mul_f32_e32 v172, 0x3e0293ee, v1
	v_mov_b32_e32 v181, v136
	v_pk_add_f32 v[138:139], v[180:181], v[172:173]
	v_mov_b32_e32 v4, 1.0
	v_cmp_gt_f32_e32 vcc, v138, v139
	s_cbranch_vccz .LBB0_1233
	ds_bpermute_b32 v1, v245, v138
	v_max_f32_e32 v2, v138, v138
	v_mov_b32_e32 v139, v137
	s_waitcnt lgkmcnt(0)
	v_max_f32_e32 v1, v1, v1
	v_max_f32_e32 v1, v2, v1
	ds_bpermute_b32 v2, v246, v1
	s_waitcnt lgkmcnt(0)
	v_max3_f32 v138, v136, v1, v2
	v_sub_f32_e32 v1, v136, v138
	v_exp_f32_e32 v194, v1
	v_mov_b32_e32 v136, v138
	s_branch .LBB0_1234
